# speedup vs baseline: 1.0186x; 1.0186x over previous
_Z16sum_layer_kernelPKfS0_Pf:
	s_load_dwordx4 s[4:7], s[0:1], 0x0
	s_load_dwordx2 s[8:9], s[0:1], 0x10
	v_and_b32_e32 v40, 31, v0
	v_bfe_u32 v41, v0, 5, 1
	v_lshrrev_b32_e32 v42, 6, v0
	v_and_b32_e32 v43, 7, v0
	v_bfe_u32 v44, v0, 3, 3
	v_and_b32_e32 v45, 63, v0
	s_lshl_b32 s3, s2, 12
	s_lshl_b32 s19, s2, 7
	v_lshlrev_b32_e32 v1, 11, v41
	v_lshl_or_b32 v1, v40, 2, v1
	v_lshlrev_b32_e32 v46, 4, v43
	v_lshl_add_u32 v35, v44, 16, v46
	v_lshl_add_u32 v35, v42, 21, v35
	v_add_u32_e32 v35, s19, v35
	v_lshlrev_b32_e32 v36, 2, v40
	v_lshl_add_u32 v36, v41, 18, v36
	v_lshl_add_u32 v36, v42, 21, v36
	v_add_u32_e32 v36, s19, v36
	v_mul_u32_u24_e32 v37, 0x1200, v42
	v_mul_u32_u24_e32 v38, 0x90, v44
	v_add3_u32 v38, v37, v38, v46
	v_mul_u32_u24_e32 v39, 0x90, v40
	v_lshlrev_b32_e32 v47, 6, v41
	v_add3_u32 v39, v37, v39, v47
	v_lshrrev_b32_e32 v46, 1, v44
	v_xor_b32_e32 v46, v43, v46
	v_lshlrev_b32_e32 v46, 4, v46
	v_lshl_add_u32 v35, v44, 16, v46
	v_lshl_add_u32 v35, v42, 21, v35
	v_add_u32_e32 v35, s19, v35
	v_xor_b32_e32 v86, 64, v35
	v_readfirstlane_b32 s23, v42
	v_bfe_u32 v47, v40, 1, 3
	v_lshlrev_b32_e32 v39, 2, v41
	v_xor_b32_e32 v39, v39, v47
	s_lshl_b32 s23, s23, 12
	v_lshlrev_b32_e32 v39, 4, v39
	v_lshl_add_u32 v39, v40, 7, v39
	v_lshl_add_u32 v39, v42, 12, v39
	s_mov_b32 m0, s23
	v_xor_b32_e32 v81, 16, v39
	v_xor_b32_e32 v82, 32, v39
	v_xor_b32_e32 v83, 48, v39
	v_cmp_gt_u32_e32 vcc, 32, v45
	v_mov_b32_e32 v34, 0xc1600000
	s_mov_b32 s16, 0x3fb8aa3b
	s_mov_b32 s17, 0x3f317218
	s_mov_b32 s20, 0x7fc00
	s_mov_b32 s21, 0xff800
	s_mov_b32 s22, 0x17f400
	s_lshl_b32 s24, 1, 16
	s_lshl_b32 s25, 2, 16
	s_lshl_b32 s26, 3, 16
	s_lshl_b32 s27, 8, 16
	s_lshl_b32 s28, 9, 16
	s_lshl_b32 s29, 10, 16
	s_lshl_b32 s30, 11, 16
	s_lshl_b32 s31, 16, 16
	s_lshl_b32 s32, 17, 16
	s_lshl_b32 s33, 18, 16
	s_lshl_b32 s34, 19, 16
	s_lshl_b32 s35, 24, 16
	s_lshl_b32 s36, 25, 16
	s_lshl_b32 s37, 26, 16
	s_lshl_b32 s38, 27, 16
	s_mov_b32 s14, 0x200000
	s_mov_b32 s15, 0x20000
	s_waitcnt lgkmcnt(0)
	s_mov_b32 s12, s6
	s_and_b32 s13, s7, 0xffff
	s_and_b32 s5, s5, 0xffff
	s_mov_b32 s6, 0x800000
	s_mov_b32 s7, s15
	s_and_b32 s9, s9, 0xffff
	s_mov_b32 s10, s6
	s_mov_b32 s11, s15
	buffer_load_dword v18, v1, s[12:15], s3 offen nt
	buffer_load_dword v19, v1, s[12:15], s3 offen offset:128 nt
	buffer_load_dword v20, v1, s[12:15], s3 offen offset:256 nt
	buffer_load_dword v21, v1, s[12:15], s3 offen offset:384 nt
	buffer_load_dword v22, v1, s[12:15], s3 offen offset:512 nt
	buffer_load_dword v23, v1, s[12:15], s3 offen offset:640 nt
	buffer_load_dword v24, v1, s[12:15], s3 offen offset:768 nt
	buffer_load_dword v25, v1, s[12:15], s3 offen offset:896 nt
	buffer_load_dword v26, v1, s[12:15], s3 offen offset:1024 nt
	buffer_load_dword v27, v1, s[12:15], s3 offen offset:1152 nt
	buffer_load_dword v28, v1, s[12:15], s3 offen offset:1280 nt
	buffer_load_dword v29, v1, s[12:15], s3 offen offset:1408 nt
	buffer_load_dword v30, v1, s[12:15], s3 offen offset:1536 nt
	buffer_load_dword v31, v1, s[12:15], s3 offen offset:1664 nt
	buffer_load_dword v32, v1, s[12:15], s3 offen offset:1792 nt
	buffer_load_dword v33, v1, s[12:15], s3 offen offset:1920 nt
	buffer_load_dwordx4 v35, s[4:7], 0 offen nt lds
	buffer_load_dwordx4 v86, s[4:7], s20 offen offset:1024 nt lds
	buffer_load_dwordx4 v35, s[4:7], s21 offen offset:2048 nt lds
	buffer_load_dwordx4 v86, s[4:7], s22 offen offset:3072 nt lds
	s_waitcnt vmcnt(4)
	v_max3_f32 v49, v18, v19, v20
	v_max3_f32 v50, v21, v22, v23
	v_max3_f32 v49, v49, v24, v25
	v_max3_f32 v50, v50, v26, v27
	v_max3_f32 v49, v49, v28, v29
	v_max3_f32 v50, v50, v30, v31
	v_max3_f32 v49, v49, v32, v33
	v_max_f32_e32 v49, v49, v50
	v_mov_b32_e32 v50, v49
	s_nop 1
	v_permlane32_swap_b32_e32 v49, v50
	v_max_f32_e32 v49, v49, v50
	v_fmamk_f32 v49, v49, 0x3fb8aa3b, v34
	v_fma_f32 v18, v18, s16, -v49
	v_exp_f32_e32 v18, v18
	v_fma_f32 v19, v19, s16, -v49
	v_exp_f32_e32 v19, v19
	v_fma_f32 v20, v20, s16, -v49
	v_exp_f32_e32 v20, v20
	v_fma_f32 v21, v21, s16, -v49
	v_exp_f32_e32 v21, v21
	v_fma_f32 v22, v22, s16, -v49
	v_exp_f32_e32 v22, v22
	v_fma_f32 v23, v23, s16, -v49
	v_exp_f32_e32 v23, v23
	v_fma_f32 v24, v24, s16, -v49
	v_exp_f32_e32 v24, v24
	v_fma_f32 v25, v25, s16, -v49
	v_exp_f32_e32 v25, v25
	v_fma_f32 v26, v26, s16, -v49
	v_exp_f32_e32 v26, v26
	v_fma_f32 v27, v27, s16, -v49
	v_exp_f32_e32 v27, v27
	v_fma_f32 v28, v28, s16, -v49
	v_exp_f32_e32 v28, v28
	v_fma_f32 v29, v29, s16, -v49
	v_exp_f32_e32 v29, v29
	v_fma_f32 v30, v30, s16, -v49
	v_exp_f32_e32 v30, v30
	v_fma_f32 v31, v31, s16, -v49
	v_exp_f32_e32 v31, v31
	v_fma_f32 v32, v32, s16, -v49
	v_exp_f32_e32 v32, v32
	v_fma_f32 v33, v33, s16, -v49
	v_exp_f32_e32 v33, v33
	v_add_f32_e32 v50, v18, v19
	v_add_f32_e32 v51, v20, v21
	v_add_f32_e32 v50, v50, v22
	v_add_f32_e32 v51, v51, v23
	v_add_f32_e32 v50, v50, v24
	v_add_f32_e32 v51, v51, v25
	v_add_f32_e32 v50, v50, v26
	v_add_f32_e32 v51, v51, v27
	v_add_f32_e32 v50, v50, v28
	v_add_f32_e32 v51, v51, v29
	v_add_f32_e32 v50, v50, v30
	v_add_f32_e32 v51, v51, v31
	v_add_f32_e32 v50, v50, v32
	v_add_f32_e32 v51, v51, v33
	v_add_f32_e32 v50, v50, v51
	v_mov_b32_e32 v51, v50
	s_nop 1
	v_permlane32_swap_b32_e32 v50, v51
	v_add_f32_e32 v50, v50, v51
	v_log_f32_e32 v50, v50
	v_cvt_pk_f16_f32 v40, v18, v19
	v_cvt_pk_f16_f32 v41, v20, v21
	v_cvt_pk_f16_f32 v42, v22, v23
	v_cvt_pk_f16_f32 v43, v24, v25
	v_cvt_pk_f16_f32 v44, v26, v27
	v_cvt_pk_f16_f32 v45, v28, v29
	v_cvt_pk_f16_f32 v46, v30, v31
	v_cvt_pk_f16_f32 v47, v32, v33
	v_add_f32_e32 v50, 0x41600000, v50
	v_mul_f32_e32 v50, 0xbf317218, v50
	v_cndmask_b32_e64 v51, v50, 1.0, vcc
	s_waitcnt vmcnt(0)
	ds_read_b128 v[2:5], v39
	ds_read_b128 v[6:9], v81
	ds_read_b128 v[10:13], v82
	ds_read_b128 v[14:17], v83
	s_waitcnt lgkmcnt(2)
	v_max3_f32 v52, v2, v3, v4
	v_max3_f32 v53, v5, v6, v7
	v_max_f32_e32 v52, v52, v8
	v_max_f32_e32 v53, v53, v9
	s_waitcnt lgkmcnt(0)
	v_max3_f32 v52, v52, v10, v11
	v_max3_f32 v53, v53, v12, v13
	v_max3_f32 v52, v52, v14, v15
	v_max3_f32 v53, v53, v16, v17
	v_max_f32_e32 v52, v52, v53
	v_mov_b32_e32 v53, v52
	s_nop 1
	v_permlane32_swap_b32_e32 v52, v53
	v_max_f32_e32 v52, v52, v53
	v_cndmask_b32_e32 v54, 1.0, v52, vcc
	v_fmamk_f32 v55, v52, 0x3fb8aa3b, v34
	v_fma_f32 v2, v2, s16, -v55
	v_mfma_f32_32x32x2_f32 v[64:79], v54, v51, 0
	v_exp_f32_e32 v2, v2
	v_fma_f32 v3, v3, s16, -v55
	v_exp_f32_e32 v3, v3
	v_fma_f32 v4, v4, s16, -v55
	v_exp_f32_e32 v4, v4
	v_fma_f32 v5, v5, s16, -v55
	v_exp_f32_e32 v5, v5
	v_fma_f32 v6, v6, s16, -v55
	v_exp_f32_e32 v6, v6
	v_fma_f32 v7, v7, s16, -v55
	v_exp_f32_e32 v7, v7
	v_fma_f32 v8, v8, s16, -v55
	v_exp_f32_e32 v8, v8
	v_fma_f32 v9, v9, s16, -v55
	v_exp_f32_e32 v9, v9
	v_fma_f32 v10, v10, s16, -v55
	v_exp_f32_e32 v10, v10
	v_cvt_pk_f16_f32 v56, v2, v3
	v_cvt_pk_f16_f32 v57, v4, v5
	v_cvt_pk_f16_f32 v58, v6, v7
	v_cvt_pk_f16_f32 v59, v8, v9
	v_fma_f32 v11, v11, s16, -v55
	v_exp_f32_e32 v11, v11
	v_fma_f32 v12, v12, s16, -v55
	v_exp_f32_e32 v12, v12
	v_mfma_f32_32x32x16_f16 v[18:33], v[56:59], v[40:43], 0
	v_fma_f32 v13, v13, s16, -v55
	v_exp_f32_e32 v13, v13
	v_fma_f32 v14, v14, s16, -v55
	v_exp_f32_e32 v14, v14
	v_fma_f32 v15, v15, s16, -v55
	v_exp_f32_e32 v15, v15
	v_fma_f32 v16, v16, s16, -v55
	v_exp_f32_e32 v16, v16
	v_fma_f32 v17, v17, s16, -v55
	v_exp_f32_e32 v17, v17
	v_cvt_pk_f16_f32 v60, v10, v11
	v_cvt_pk_f16_f32 v61, v12, v13
	v_cvt_pk_f16_f32 v62, v14, v15
	v_cvt_pk_f16_f32 v63, v16, v17
	s_nop 1
	v_mfma_f32_32x32x16_f16 v[18:33], v[60:63], v[44:47], v[18:33]
	s_nop 11
	v_log_f32_e32 v18, v18
	v_log_f32_e32 v19, v19
	v_log_f32_e32 v20, v20
	v_fmac_f32_e32 v64, s17, v18
	buffer_store_dword v64, v36, s[8:11], 0 offen
	v_log_f32_e32 v21, v21
	v_fmac_f32_e32 v65, s17, v19
	buffer_store_dword v65, v36, s[8:11], s24 offen
	v_log_f32_e32 v22, v22
	v_fmac_f32_e32 v66, s17, v20
	buffer_store_dword v66, v36, s[8:11], s25 offen
	v_log_f32_e32 v23, v23
	v_fmac_f32_e32 v67, s17, v21
	buffer_store_dword v67, v36, s[8:11], s26 offen
	v_log_f32_e32 v24, v24
	v_fmac_f32_e32 v68, s17, v22
	buffer_store_dword v68, v36, s[8:11], s27 offen
	v_log_f32_e32 v25, v25
	v_fmac_f32_e32 v69, s17, v23
	buffer_store_dword v69, v36, s[8:11], s28 offen
	v_log_f32_e32 v26, v26
	v_fmac_f32_e32 v70, s17, v24
	buffer_store_dword v70, v36, s[8:11], s29 offen
	v_log_f32_e32 v27, v27
	v_fmac_f32_e32 v71, s17, v25
	buffer_store_dword v71, v36, s[8:11], s30 offen
	v_log_f32_e32 v28, v28
	v_fmac_f32_e32 v72, s17, v26
	buffer_store_dword v72, v36, s[8:11], s31 offen
	v_log_f32_e32 v29, v29
	v_fmac_f32_e32 v73, s17, v27
	buffer_store_dword v73, v36, s[8:11], s32 offen
	v_log_f32_e32 v30, v30
	v_fmac_f32_e32 v74, s17, v28
	buffer_store_dword v74, v36, s[8:11], s33 offen
	v_log_f32_e32 v31, v31
	v_fmac_f32_e32 v75, s17, v29
	buffer_store_dword v75, v36, s[8:11], s34 offen
	v_log_f32_e32 v32, v32
	v_fmac_f32_e32 v76, s17, v30
	buffer_store_dword v76, v36, s[8:11], s35 offen
	v_log_f32_e32 v33, v33
	v_fmac_f32_e32 v77, s17, v31
	buffer_store_dword v77, v36, s[8:11], s36 offen
	v_fmac_f32_e32 v78, s17, v32
	buffer_store_dword v78, v36, s[8:11], s37 offen
	v_fmac_f32_e32 v79, s17, v33
	buffer_store_dword v79, v36, s[8:11], s38 offen
	s_endpgm

	.amdhsa_kernel _Z16sum_layer_kernelPKfS0_Pf
		.amdhsa_group_segment_fixed_size 18432
		.amdhsa_private_segment_fixed_size 0
		.amdhsa_kernarg_size 24
		.amdhsa_user_sgpr_count 2
		.amdhsa_user_sgpr_dispatch_ptr 0
		.amdhsa_user_sgpr_queue_ptr 0
		.amdhsa_user_sgpr_kernarg_segment_ptr 1
		.amdhsa_user_sgpr_dispatch_id 0
		.amdhsa_user_sgpr_kernarg_preload_length 0
		.amdhsa_user_sgpr_kernarg_preload_offset 0
		.amdhsa_user_sgpr_private_segment_size 0
		.amdhsa_uses_dynamic_stack 0
		.amdhsa_enable_private_segment 0
		.amdhsa_system_sgpr_workgroup_id_x 1
		.amdhsa_system_sgpr_workgroup_id_y 0
		.amdhsa_system_sgpr_workgroup_id_z 0
		.amdhsa_system_sgpr_workgroup_info 0
		.amdhsa_system_vgpr_workitem_id 0
		.amdhsa_next_free_vgpr 88
		.amdhsa_next_free_sgpr 39
		.amdhsa_accum_offset 88
		.amdhsa_reserve_vcc 1
		.amdhsa_float_round_mode_32 0
		.amdhsa_float_round_mode_16_64 0
		.amdhsa_float_denorm_mode_32 3
		.amdhsa_float_denorm_mode_16_64 3
		.amdhsa_dx10_clamp 1
		.amdhsa_ieee_mode 1
		.amdhsa_fp16_overflow 0
		.amdhsa_tg_split 0
		.amdhsa_exception_fp_ieee_invalid_op 0
		.amdhsa_exception_fp_denorm_src 0
		.amdhsa_exception_fp_ieee_div_zero 0
		.amdhsa_exception_fp_ieee_overflow 0
		.amdhsa_exception_fp_ieee_underflow 0
		.amdhsa_exception_fp_ieee_inexact 0
		.amdhsa_exception_int_div_zero 0
	.end_amdhsa_kernel

amdhsa.kernels:
  - .agpr_count:     0
    .args:
      - .address_space:  global
        .offset:         0
        .size:           8
        .value_kind:     global_buffer
      - .address_space:  global
        .offset:         8
        .size:           8
        .value_kind:     global_buffer
      - .address_space:  global
        .offset:         16
        .size:           8
        .value_kind:     global_buffer
    .group_segment_fixed_size: 18432
    .kernarg_segment_align: 8
    .kernarg_segment_size: 24
    .language:       OpenCL C
    .language_version:
      - 2
      - 0
    .max_flat_workgroup_size: 256
    .name:           _Z16sum_layer_kernelPKfS0_Pf
    .private_segment_fixed_size: 0
    .sgpr_count:     45
    .sgpr_spill_count: 0
    .symbol:         _Z16sum_layer_kernelPKfS0_Pf.kd
    .uniform_work_group_size: 1
    .uses_dynamic_stack: false
    .vgpr_count:     88
    .vgpr_spill_count: 0
    .wavefront_size: 64
